# DATT: waves 4..7 stage the next K/V tile before their compute, waves 0..3 after (phase offset between the two waves of a SIMD)
# baseline (speedup 1.0000x reference)
; __device__ __forceinline__ void datt_stream(LAS unsigned char* lds, const DattRun& c, const float C, const int wv) {
;     const int NP = c.np, NS = NP + 2; constexpr int HALFWIN = 64;
;     const int tid = otid(wv), wid = __builtin_amdgcn_readfirstlane(tid >> 6), lane = tid & 63, r32 = lane & 31, hi = lane >> 5, par = wid & 1, pa0 = wid >> 1;
;     LAS unsigned char* V_lds = lds; LAS unsigned char* K_lds = lds + 2 * SHM_T; LAS unsigned char* stg = lds + 65536 + wid * 8192;
;     LAS float* wsf = (LAS float*)(lds + 132096) + wid * 64; LAS float* li_l = wsf; LAS float* al_l = wsf + 32;
;     auto rowoff = [&](int idx) __attribute__((always_inline)) { return (size_t)(idx * c.dil + c.r) * ODD_IN + c.g * 3072 + c.h * 128; };
;     const bool edge = (c.a0 == 0) || (64 * (c.a0 + NP) >= c.L);
;     const int sr = tid >> 4, sc = (tid & 15) * 8;
;     const int vst0 = v_st(sr, sc), vst1 = v_st(32 + sr, sc), kst0 = ATT_KSWZ(sr, sc * 2), kst1 = ATT_KSWZ(32 + sr, sc * 2);
;     const int vb0 = (int)(unsigned)(uintptr_t)V_lds + v_rd_base(lane);
;     u32x2 ksA0, ksA1, vsA0, vsA1, ksB0, ksB1, vsB0, vsB1;
;     const unsigned char* zb = c.z + c.g * 3072 + c.h * 128;
;     auto roff = [&](int idx) __attribute__((always_inline)) { return (unsigned)(idx * c.dil + c.r) * (unsigned)ODD_IN; };
; template <int PH, bool PRB = false>
; __device__ __forceinline__ void run_phase(int layer, LAS unsigned char* lds, const int wv_) {
;     ...
;     if constexpr (PH == PH_DATT) {
;         float* lse = (float*)(ws + WS_MISC + MISC_LSE);
;         LAS float* tb = (LAS float*)(lds + 132096 + 4096);
;         for (int it = bid; it < 512; it += G) {
;             const bool dbl = it < 256; const int g = dbl ? (it >> 7) : 2, cc = dbl ? (it & 127) : (it - 256), hh = cc & 7, rest = cc >> 3;
;             const int dil = g == 0 ? 1 : (g == 1 ? 4 : 16), r = rest % dil, chunk = rest / dil;
;             { const int t2 = otid(wv); if (t2 < 256) { const int d = t2 - 128; tb[t2] = (d >= -64 && d <= 64) ? bto[(g * 8 + hh) * 129 + d + 64] * 1.4426950408889634f : -__builtin_inff(); } }
;             att::DattRun R{ws + WS_Z, (bf16*)(ws + WS_Z + Z_OB), PRB ? (float*)(ws + WS_H + 26 * MiB) : lse, tb, g, hh, dil, r, chunk * (dbl ? 16 : 8), S / dil, PRB ? y : nullptr, dbl ? 16 : 8};
;             att::datt_stream(lds, R, 0.08838834764831845f * 1.4426950408889634f, wv);
.LBB0_403:
	s_bitcmp1_b32 s80, 0
	s_cselect_b64 s[2:3], -1, 0
	s_mov_b64 s[0:1], -1
	s_and_b64 vcc, exec, s[2:3]
	v_writelane_b32 v255, s80, 1
	s_waitcnt lgkmcnt(0)
	s_barrier
	s_cbranch_vccz .LBB0_636
	s_mov_b64 s[0:1], 0
	s_mov_b32 s100, 0
	s_mov_b32 s101, 0
	v_readlane_b32 s98, v254, 8
	s_mov_b32 s99, 0
	s_cmp_ge_u32 s98, 4
	s_cselect_b32 s98, 1, 0
	s_mov_b32 s2, s80
	v_mbcnt_lo_u32_b32 v0, -1, 0
	v_mbcnt_hi_u32_b32 v0, -1, v0
	v_readlane_b32 s50, v254, 0
	v_add_u32_e32 v0, s93, v0
	s_cmpk_gt_i32 s50, 0x1ff
	s_cbranch_scc1 .LBB0_524
	v_readlane_b32 s2, v254, 1
	v_readlane_b32 s3, v254, 2
	s_add_u32 s0, s2, s0
	s_addc_u32 s1, s3, s1
	s_load_dwordx2 s[0:1], s[0:1], 0xe0
	s_waitcnt lgkmcnt(0)
	s_add_u32 s2, s0, 0x8100000
	v_writelane_b32 v255, s2, 2
	s_addc_u32 s2, s1, 0
	v_writelane_b32 v255, s2, 3
	s_add_u32 s2, s0, 0x21c00000
	v_writelane_b32 v255, s2, 4
	s_addc_u32 s2, s1, 0
	v_writelane_b32 v255, s2, 5
	s_add_u32 s2, s0, 0x11100000
	v_writelane_b32 v255, s2, 6
	v_writelane_b32 v255, s0, 7
	s_nop 1
	v_writelane_b32 v255, s1, 8
	s_addc_u32 s0, s1, 0
	v_writelane_b32 v255, s0, 9
	s_branch .LBB0_407

; #define DS_LOADQ(pa) do { const unsigned _q = roff(64 * (c.a0 + (pa)) + 32 * par + r32) + (unsigned)hi * 8u; _Pragma("unroll") for (int d0 = 0; d0 < 8; ++d0) qraw[d0] = *(const u32x2*)(zb + (_q + d0 * 16u)); } while (0)
; #define DS_RESET() do { m_reg = -1e30f; l_reg = 0.f; _Pragma("unroll") for (int d = 0; d < 4; ++d) _Pragma("unroll") for (int r = 0; r < 16; ++r) o[d][r] = 0.f; } while (0)
; __device__ __forceinline__ void datt_stream(LAS unsigned char* lds, const DattRun& c, const float C, const int wv) {
;     ...
;     auto finish = [&](const int pa) __attribute__((always_inline)) {
;         if (hi == 0) li_l[r32] = l_reg; asm volatile("s_waitcnt lgkmcnt(0)" ::: "memory");
;         const int i0 = 64 * (c.a0 + pa) + 32 * par;
;         if (hi == 0) c.lse[((size_t)c.g * S + (size_t)(i0 + r32) * c.dil + c.r) * 8 + c.h] = (m_reg + __builtin_amdgcn_logf(l_reg)) * 0.6931471805599453f;
;     ...
; #pragma unroll 1
;     for (int s = 0; s < NS + 2; s += 2) {
; #pragma unroll
;         for (int q = 0; q < 2; ++q) {
;             const int st = s + q, dd = st - pa0, rel = dd & 3, pa = pa0 + 4 * (dd >> 2); const bool act = dd >= 0 && pa < NP;
;             if (st > NS) break;
;             if (act && rel <= 2) { compute(rel, q, pa); if (rel == 2 && pa + 4 < NP) DS_LOADQ(pa + 4); }
;             else if (act) { finish(pa); DS_RESET(); }
.LBB0_413:
	s_mov_b32 s99, 0
	s_add_i32 s54, s58, s57
	s_and_b32 s55, s54, -4
	s_and_b32 s62, s54, 3
	s_add_i32 s55, s55, s49
	s_cmp_gt_i32 s54, -1
	s_cselect_b64 s[0:1], -1, 0
	s_cmp_lt_i32 s55, s61
	s_cselect_b64 s[6:7], -1, 0
	s_and_b64 s[6:7], s[0:1], s[6:7]
	s_xor_b64 s[8:9], s[6:7], -1
	s_cmp_eq_u32 s62, 3
	s_cselect_b64 s[10:11], -1, 0
	s_or_b64 s[8:9], s[10:11], s[8:9]
	s_mov_b64 s[0:1], -1
	s_and_b64 vcc, exec, s[8:9]
	s_cbranch_vccz .LBB0_421
	v_mov_b64_e32 v[94:95], v[14:15]
	v_mov_b64_e32 v[110:111], v[30:31]
	v_mov_b64_e32 v[126:127], v[46:47]
	v_mov_b64_e32 v[142:143], v[62:63]
	s_andn2_b64 vcc, exec, s[6:7]
	v_mov_b32_e32 v244, v246
	v_mov_b32_e32 v243, v245
	v_mov_b64_e32 v[92:93], v[12:13]
	v_mov_b64_e32 v[90:91], v[10:11]
	v_mov_b64_e32 v[88:89], v[8:9]
	v_mov_b64_e32 v[86:87], v[6:7]
	v_mov_b64_e32 v[84:85], v[4:5]
	v_mov_b64_e32 v[82:83], v[2:3]
	v_mov_b64_e32 v[80:81], v[0:1]
	v_mov_b64_e32 v[108:109], v[28:29]
	v_mov_b64_e32 v[106:107], v[26:27]
	v_mov_b64_e32 v[104:105], v[24:25]
	v_mov_b64_e32 v[102:103], v[22:23]
	v_mov_b64_e32 v[100:101], v[20:21]
	v_mov_b64_e32 v[98:99], v[18:19]
	v_mov_b64_e32 v[96:97], v[16:17]
	v_mov_b64_e32 v[124:125], v[44:45]
	v_mov_b64_e32 v[122:123], v[42:43]
	v_mov_b64_e32 v[120:121], v[40:41]
	v_mov_b64_e32 v[118:119], v[38:39]
	v_mov_b64_e32 v[116:117], v[36:37]
	v_mov_b64_e32 v[114:115], v[34:35]
	v_mov_b64_e32 v[112:113], v[32:33]
	v_mov_b64_e32 v[140:141], v[60:61]
	v_mov_b64_e32 v[138:139], v[58:59]
	v_mov_b64_e32 v[136:137], v[56:57]
	v_mov_b64_e32 v[134:135], v[54:55]
	v_mov_b64_e32 v[132:133], v[52:53]
	v_mov_b64_e32 v[130:131], v[50:51]
	v_mov_b64_e32 v[128:129], v[48:49]
	s_cbranch_vccnz .LBB0_420
	s_and_saveexec_b64 s[0:1], s[4:5]
	ds_write_b32 v229, v246
	s_or_b64 exec, exec, s[0:1]
	s_waitcnt lgkmcnt(0)
	s_add_i32 s0, s55, s48
	s_lshl_b32 s0, s0, 6
	s_or_b32 s6, s0, s80
	s_and_saveexec_b64 s[0:1], s[4:5]
	s_cbranch_execz .LBB0_419
	v_log_f32_e32 v64, v246
	v_or_b32_e32 v66, s6, v222
	v_ashrrev_i32_e32 v67, 31, v66
	v_lshlrev_b64 v[66:67], s45, v[66:67]
	v_lshl_add_u64 v[66:67], v[66:67], 0, s[2:3]
	v_add_f32_e32 v64, v245, v64
	v_lshlrev_b64 v[66:67], 5, v[66:67]
	v_mul_f32_e32 v64, 0x3f317218, v64
	v_lshl_add_u64 v[66:67], s[46:47], 0, v[66:67]
	global_store_dword v[66:67], v64, off

; #define DS_LOADQ(pa) do { const unsigned _q = roff(64 * (c.a0 + (pa)) + 32 * par + r32) + (unsigned)hi * 8u; _Pragma("unroll") for (int d0 = 0; d0 < 8; ++d0) qraw[d0] = *(const u32x2*)(zb + (_q + d0 * 16u)); } while (0)
; __device__ __forceinline__ void datt_stream(LAS unsigned char* lds, const DattRun& c, const float C, const int wv) {
;     ...
;     auto compute = [&](const int rel, const int b, const int pa) __attribute__((always_inline)) {
;         const int tr = edge ? 0 : (rel == 1 ? 1 : (par ? (rel == 0 ? 2 : 0) : (rel == 2 ? 3 : 0))); const bool do0 = tr != 2, do1 = tr != 3;
;         if (rel == 0) {
; #pragma unroll
;             for (int d0 = 0; d0 < 8; ++d0) qr[d0] = f8tob(qraw[d0]); }
;     ...
;             const int st = s + q, dd = st - pa0, rel = dd & 3, pa = pa0 + 4 * (dd >> 2); const bool act = dd >= 0 && pa < NP;
;             if (st > NS) break;
;             if (act && rel <= 2) { compute(rel, q, pa); if (rel == 2 && pa + 4 < NP) DS_LOADQ(pa + 4); }
.LBB0_421:
	s_andn2_b64 vcc, exec, s[0:1]
	s_cbranch_vccnz .LBB0_467
	s_cmp_eq_u32 s98, 0
	s_cbranch_scc1 .LtaN0
	s_mov_b32 s99, 1
	s_branch .LtaE0
.LtaN0:
	s_add_i32 s6, s55, s48
	s_add_i32 s6, s6, s62
	s_lshl_b32 s6, s6, 6
	s_addk_i32 s6, 0xffc0
	s_cmp_lt_u32 s6, s44
	s_cselect_b64 s[10:11], -1, 0
	s_or_b64 s[10:11], s[10:11], s[64:65]
	s_andn2_b64 vcc, exec, s[10:11]
	s_not_b64 s[10:11], s[10:11]
	s_mov_b32 s6, 0
	s_cbranch_vccnz .LBB0_428
	s_cmp_eq_u32 s62, 1
	s_mov_b32 s6, 1
	s_cbranch_scc1 .LBB0_428
	v_readlane_b32 s0, v254, 63
	v_readlane_b32 s1, v255, 0
	s_andn2_b64 vcc, exec, s[0:1]
	s_mov_b64 s[0:1], -1
	s_cbranch_vccnz .LBB0_426
	s_cmp_eq_u32 s62, 0
	s_cselect_b32 s6, 2, 0
	s_mov_b64 s[0:1], 0

; #define DS_LOAD(X, s) do { const int _s = (s) < NS - 1 ? (s) : NS - 1; const int _j = 64 * (c.a0 - 1 + _s) + sr; const unsigned _k0 = DS_KROW(_j) + (unsigned)sc, _k1 = DS_KROW(_j + 32) + (unsigned)sc; \
;         ks##X##0 = *(const u32x2*)(zb + _k0); vs##X##0 = *(const u32x2*)(zb + (_k0 + 1024u)); ks##X##1 = *(const u32x2*)(zb + _k1); vs##X##1 = *(const u32x2*)(zb + (_k1 + 1024u)); } while (0)
; #define DS_WRITE(X, b) do { *(LAS bf16x8*)(V_lds + (b) * SHM_T + vst0) = f8tob(vs##X##0); *(LAS bf16x8*)(K_lds + (b) * SHM_T + kst0) = f8tob(ks##X##0); \
;         *(LAS bf16x8*)(V_lds + (b) * SHM_T + vst1) = f8tob(vs##X##1); *(LAS bf16x8*)(K_lds + (b) * SHM_T + kst1) = f8tob(ks##X##1); } while (0)
; #define DS_LOADQ(pa) do { const unsigned _q = roff(64 * (c.a0 + (pa)) + 32 * par + r32) + (unsigned)hi * 8u; _Pragma("unroll") for (int d0 = 0; d0 < 8; ++d0) qraw[d0] = *(const u32x2*)(zb + (_q + d0 * 16u)); } while (0)
; #define DS_RESET() do { m_reg = -1e30f; l_reg = 0.f; _Pragma("unroll") for (int d = 0; d < 4; ++d) _Pragma("unroll") for (int r = 0; r < 16; ++r) o[d][r] = 0.f; } while (0)
; __device__ __forceinline__ void datt_stream(LAS unsigned char* lds, const DattRun& c, const float C, const int wv) {
;     ...
;     bf16x8 qr[8]; u32x2 qraw[8]; float m_reg = -1e30f, l_reg = 0.f; f32x16 o[4];
;     ...
;     DS_LOADQ(pa0); DS_RESET();
;     auto compute = [&](const int rel, const int b, const int pa) __attribute__((always_inline)) {
;         const int tr = edge ? 0 : (rel == 1 ? 1 : (par ? (rel == 0 ? 2 : 0) : (rel == 2 ? 3 : 0))); const bool do0 = tr != 2, do1 = tr != 3;
;         if (rel == 0) {
; #pragma unroll
;             for (int d0 = 0; d0 < 8; ++d0) qr[d0] = f8tob(qraw[d0]); }
;     ...
;             if (q == 0) { DS_WRITE(A, 1); DS_LOAD(A, st + 3); } else { DS_WRITE(B, 0); DS_LOAD(B, st + 3); }
.LBB0_467:
	s_cmp_eq_u32 s99, 1
	s_cbranch_scc1 .LtaB0
.LtaE0:
	s_waitcnt vmcnt(4)
	v_cvt_scalef32_pk_bf16_fp8 v66, v206, 1.0
	v_cvt_scalef32_pk_bf16_fp8 v67, v206, 1.0 op_sel:[1,0,0]
	v_cvt_scalef32_pk_bf16_fp8 v68, v207, 1.0
	v_cvt_scalef32_pk_bf16_fp8 v69, v207, 1.0 op_sel:[1,0,0]
	ds_write_b128 v225, v[66:69] offset:16384
	s_waitcnt vmcnt(4)
	v_cvt_scalef32_pk_bf16_fp8 v66, v202, 1.0
	v_cvt_scalef32_pk_bf16_fp8 v67, v202, 1.0 op_sel:[1,0,0]
	v_cvt_scalef32_pk_bf16_fp8 v68, v203, 1.0
	v_cvt_scalef32_pk_bf16_fp8 v69, v203, 1.0 op_sel:[1,0,0]
	ds_write_b128 v226, v[66:69] offset:49152
	s_waitcnt vmcnt(4)
	v_cvt_scalef32_pk_bf16_fp8 v66, v198, 1.0
	v_cvt_scalef32_pk_bf16_fp8 v67, v198, 1.0 op_sel:[1,0,0]
	v_cvt_scalef32_pk_bf16_fp8 v68, v199, 1.0
	v_cvt_scalef32_pk_bf16_fp8 v69, v199, 1.0 op_sel:[1,0,0]
	s_add_i32 s0, s57, 3
	ds_write_b128 v227, v[66:69] offset:16384
	s_waitcnt vmcnt(4)
	s_min_i32 s0, s0, s81
	v_cvt_scalef32_pk_bf16_fp8 v66, v194, 1.0
	v_cvt_scalef32_pk_bf16_fp8 v67, v194, 1.0 op_sel:[1,0,0]
	v_cvt_scalef32_pk_bf16_fp8 v68, v195, 1.0
	v_add_u32_e32 v70, s0, v224
	v_cvt_scalef32_pk_bf16_fp8 v69, v195, 1.0 op_sel:[1,0,0]
	v_lshl_add_u32 v72, v70, 6, v197
	v_add_u32_e32 v70, 32, v72
	v_min_i32_e32 v70, s95, v70
	v_cmp_lt_i32_e32 vcc, s43, v72
	v_min_i32_e32 v73, s95, v72
	s_cmp_gt_u32 s57, s61
	v_cndmask_b32_e32 v70, 0, v70, vcc
	v_cmp_lt_i32_e32 vcc, -1, v72
	v_lshlrev_b32_e32 v70, s45, v70
	v_add_u32_e32 v70, s56, v70
	v_cndmask_b32_e32 v72, 0, v73, vcc
	v_lshlrev_b32_e32 v72, s45, v72
	v_mad_u64_u32 v[70:71], s[0:1], v70, s42, v[196:197]
	v_add_u32_e32 v72, s56, v72
	v_add_u32_e32 v71, 0x400, v70
	v_mad_u64_u32 v[72:73], s[0:1], v72, s42, v[196:197]
	v_add_u32_e32 v73, 0x400, v72
	global_load_dwordx2 v[198:199], v71, s[92:93]
	global_load_dwordx2 v[206:207], v73, s[92:93]
	global_load_dwordx2 v[202:203], v72, s[92:93]
	global_load_dwordx2 v[194:195], v70, s[92:93]
	s_cselect_b64 s[0:1], -1, 0
	s_and_b64 vcc, exec, s[0:1]
	ds_write_b128 v228, v[66:69] offset:49152
	s_cmp_eq_u32 s99, 1
	s_cbranch_scc1 .LtaN0
.LtaB0:
	s_cmp_eq_u32 s101, 2
	s_cbranch_scc0 .Ldatt_qc0_skip
	v_cvt_pk_f32_fp8_e32 v[0:1], v176
	v_cvt_pk_f32_fp8_sdwa v[2:3], v176 src0_sel:WORD_1
	v_cvt_pk_f32_fp8_e32 v[4:5], v177
	v_cvt_pk_f32_fp8_sdwa v[6:7], v177 src0_sel:WORD_1
	v_cvt_pk_bf16_f32 v144, v0, v1
	v_cvt_pk_bf16_f32 v145, v2, v3
	v_cvt_pk_bf16_f32 v146, v4, v5
	v_cvt_pk_bf16_f32 v147, v6, v7
	v_cvt_pk_f32_fp8_e32 v[0:1], v178
	v_cvt_pk_f32_fp8_sdwa v[2:3], v178 src0_sel:WORD_1
	v_cvt_pk_f32_fp8_e32 v[4:5], v179
	v_cvt_pk_f32_fp8_sdwa v[6:7], v179 src0_sel:WORD_1
	v_cvt_pk_bf16_f32 v148, v0, v1
	v_cvt_pk_bf16_f32 v149, v2, v3
	v_cvt_pk_bf16_f32 v150, v4, v5
	v_cvt_pk_bf16_f32 v151, v6, v7
	v_cvt_pk_f32_fp8_e32 v[0:1], v180
	v_cvt_pk_f32_fp8_sdwa v[2:3], v180 src0_sel:WORD_1
	v_cvt_pk_f32_fp8_e32 v[4:5], v181
	v_cvt_pk_f32_fp8_sdwa v[6:7], v181 src0_sel:WORD_1
	v_cvt_pk_bf16_f32 v152, v0, v1
	v_cvt_pk_bf16_f32 v153, v2, v3
	v_cvt_pk_bf16_f32 v154, v4, v5
	v_cvt_pk_bf16_f32 v155, v6, v7
	v_cvt_pk_f32_fp8_e32 v[0:1], v182
	v_cvt_pk_f32_fp8_sdwa v[2:3], v182 src0_sel:WORD_1
	v_cvt_pk_f32_fp8_e32 v[4:5], v183
	v_cvt_pk_f32_fp8_sdwa v[6:7], v183 src0_sel:WORD_1
	v_cvt_pk_bf16_f32 v156, v0, v1
	v_cvt_pk_bf16_f32 v157, v2, v3
	v_cvt_pk_bf16_f32 v158, v4, v5
	v_cvt_pk_bf16_f32 v159, v6, v7
	v_cvt_pk_f32_fp8_e32 v[0:1], v184
	v_cvt_pk_f32_fp8_sdwa v[2:3], v184 src0_sel:WORD_1
	v_cvt_pk_f32_fp8_e32 v[4:5], v185
	v_cvt_pk_f32_fp8_sdwa v[6:7], v185 src0_sel:WORD_1
	v_cvt_pk_bf16_f32 v160, v0, v1
	v_cvt_pk_bf16_f32 v161, v2, v3
	v_cvt_pk_bf16_f32 v162, v4, v5
	v_cvt_pk_bf16_f32 v163, v6, v7
	v_cvt_pk_f32_fp8_e32 v[0:1], v188
	v_cvt_pk_f32_fp8_sdwa v[2:3], v188 src0_sel:WORD_1
	v_cvt_pk_f32_fp8_e32 v[4:5], v189
	v_cvt_pk_f32_fp8_sdwa v[6:7], v189 src0_sel:WORD_1
	v_cvt_pk_bf16_f32 v164, v0, v1
	v_cvt_pk_bf16_f32 v165, v2, v3
	v_cvt_pk_bf16_f32 v166, v4, v5
	v_cvt_pk_bf16_f32 v167, v6, v7
	v_cvt_pk_f32_fp8_e32 v[0:1], v190
	v_cvt_pk_f32_fp8_sdwa v[2:3], v190 src0_sel:WORD_1
	v_cvt_pk_f32_fp8_e32 v[4:5], v191
	v_cvt_pk_f32_fp8_sdwa v[6:7], v191 src0_sel:WORD_1
	v_cvt_pk_bf16_f32 v168, v0, v1
	v_cvt_pk_bf16_f32 v169, v2, v3
	v_cvt_pk_bf16_f32 v170, v4, v5
	v_cvt_pk_bf16_f32 v171, v6, v7
	v_cvt_pk_f32_fp8_e32 v[0:1], v192
	v_cvt_pk_f32_fp8_sdwa v[2:3], v192 src0_sel:WORD_1
	v_cvt_pk_f32_fp8_e32 v[4:5], v193
	v_cvt_pk_f32_fp8_sdwa v[6:7], v193 src0_sel:WORD_1
	v_cvt_pk_bf16_f32 v172, v0, v1
	v_cvt_pk_bf16_f32 v173, v2, v3
	v_cvt_pk_bf16_f32 v174, v4, v5
	v_cvt_pk_bf16_f32 v175, v6, v7
	s_mov_b32 s101, 3

; #define DS_LOAD(X, s) do { const int _s = (s) < NS - 1 ? (s) : NS - 1; const int _j = 64 * (c.a0 - 1 + _s) + sr; const unsigned _k0 = DS_KROW(_j) + (unsigned)sc, _k1 = DS_KROW(_j + 32) + (unsigned)sc; \
;         ks##X##0 = *(const u32x2*)(zb + _k0); vs##X##0 = *(const u32x2*)(zb + (_k0 + 1024u)); ks##X##1 = *(const u32x2*)(zb + _k1); vs##X##1 = *(const u32x2*)(zb + (_k1 + 1024u)); } while (0)
; #define DS_WRITE(X, b) do { *(LAS bf16x8*)(V_lds + (b) * SHM_T + vst0) = f8tob(vs##X##0); *(LAS bf16x8*)(K_lds + (b) * SHM_T + kst0) = f8tob(ks##X##0); \
;         *(LAS bf16x8*)(V_lds + (b) * SHM_T + vst1) = f8tob(vs##X##1); *(LAS bf16x8*)(K_lds + (b) * SHM_T + kst1) = f8tob(ks##X##1); } while (0)
; #define DS_LOADQ(pa) do { const unsigned _q = roff(64 * (c.a0 + (pa)) + 32 * par + r32) + (unsigned)hi * 8u; _Pragma("unroll") for (int d0 = 0; d0 < 8; ++d0) qraw[d0] = *(const u32x2*)(zb + (_q + d0 * 16u)); } while (0)
; #define DS_RESET() do { m_reg = -1e30f; l_reg = 0.f; _Pragma("unroll") for (int d = 0; d < 4; ++d) _Pragma("unroll") for (int r = 0; r < 16; ++r) o[d][r] = 0.f; } while (0)
; __device__ __forceinline__ void datt_stream(LAS unsigned char* lds, const DattRun& c, const float C, const int wv) {
;     ...
;     auto finish = [&](const int pa) __attribute__((always_inline)) {
;         if (hi == 0) li_l[r32] = l_reg; asm volatile("s_waitcnt lgkmcnt(0)" ::: "memory");
;         const int i0 = 64 * (c.a0 + pa) + 32 * par;
;         if (hi == 0) c.lse[((size_t)c.g * S + (size_t)(i0 + r32) * c.dil + c.r) * 8 + c.h] = (m_reg + __builtin_amdgcn_logf(l_reg)) * 0.6931471805599453f;
;     ...
;     for (int s = 0; s < NS + 2; s += 2) {
; #pragma unroll
;         for (int q = 0; q < 2; ++q) {
;             const int st = s + q, dd = st - pa0, rel = dd & 3, pa = pa0 + 4 * (dd >> 2); const bool act = dd >= 0 && pa < NP;
;             if (st > NS) break;
;             if (act && rel <= 2) { compute(rel, q, pa); if (rel == 2 && pa + 4 < NP) DS_LOADQ(pa + 4); }
;             else if (act) { finish(pa); DS_RESET(); }
;             if (q == 0) { DS_WRITE(A, 1); DS_LOAD(A, st + 3); } else { DS_WRITE(B, 0); DS_LOAD(B, st + 3); }
;             __syncthreads();
.Ldatt_q0_skip:
	s_cmp_gt_u32 s57, s61
	s_cselect_b64 s[0:1], -1, 0
	s_and_b64 vcc, exec, s[0:1]
	s_waitcnt lgkmcnt(0)
	s_barrier
	s_cbranch_vccnz .LBB0_412
	s_mov_b32 s99, 0
	s_add_i32 s54, s54, 1
	s_and_b32 s62, s54, -4
	s_and_b32 s63, s54, 3
	s_add_i32 s62, s62, s49
	s_cmp_gt_i32 s54, -1
	s_cselect_b64 s[6:7], -1, 0
	s_cmp_lt_i32 s62, s61
	s_cselect_b64 s[8:9], -1, 0
	s_and_b64 s[8:9], s[6:7], s[8:9]
	s_cmp_lg_u32 s63, 3
	s_cselect_b64 s[6:7], -1, 0
	s_and_b64 s[10:11], s[6:7], s[8:9]
	s_mov_b64 s[6:7], -1
	s_and_b64 vcc, exec, s[10:11]
	s_cbranch_vccnz .LBB0_476
	v_mov_b64_e32 v[0:1], v[80:81]
	v_mov_b64_e32 v[16:17], v[96:97]
	v_mov_b64_e32 v[32:33], v[112:113]
	v_mov_b64_e32 v[48:49], v[128:129]
	s_andn2_b64 vcc, exec, s[8:9]
	v_mov_b32_e32 v246, v244
	v_mov_b32_e32 v245, v243
	v_mov_b64_e32 v[2:3], v[82:83]
	v_mov_b64_e32 v[4:5], v[84:85]
	v_mov_b64_e32 v[6:7], v[86:87]
	v_mov_b64_e32 v[8:9], v[88:89]
	v_mov_b64_e32 v[10:11], v[90:91]
	v_mov_b64_e32 v[12:13], v[92:93]
	v_mov_b64_e32 v[14:15], v[94:95]
	v_mov_b64_e32 v[18:19], v[98:99]
	v_mov_b64_e32 v[20:21], v[100:101]
	v_mov_b64_e32 v[22:23], v[102:103]
	v_mov_b64_e32 v[24:25], v[104:105]
	v_mov_b64_e32 v[26:27], v[106:107]
	v_mov_b64_e32 v[28:29], v[108:109]
	v_mov_b64_e32 v[30:31], v[110:111]
	v_mov_b64_e32 v[34:35], v[114:115]
	v_mov_b64_e32 v[36:37], v[116:117]
	v_mov_b64_e32 v[38:39], v[118:119]
	v_mov_b64_e32 v[40:41], v[120:121]
	v_mov_b64_e32 v[42:43], v[122:123]
	v_mov_b64_e32 v[44:45], v[124:125]
	v_mov_b64_e32 v[46:47], v[126:127]
	v_mov_b64_e32 v[50:51], v[130:131]
	v_mov_b64_e32 v[52:53], v[132:133]
	v_mov_b64_e32 v[54:55], v[134:135]
	v_mov_b64_e32 v[56:57], v[136:137]
	v_mov_b64_e32 v[58:59], v[138:139]
	v_mov_b64_e32 v[60:61], v[140:141]
	v_mov_b64_e32 v[62:63], v[142:143]
	s_cbranch_vccnz .LBB0_475
	s_and_saveexec_b64 s[6:7], s[4:5]
	ds_write_b32 v229, v244
	s_or_b64 exec, exec, s[6:7]
	s_waitcnt lgkmcnt(0)
	s_add_i32 s6, s62, s48
	s_lshl_b32 s6, s6, 6
	s_or_b32 s8, s6, s80
	s_and_saveexec_b64 s[6:7], s[4:5]
	s_cbranch_execz .LBB0_474
	v_log_f32_e32 v2, v244
	v_or_b32_e32 v0, s8, v222
	v_ashrrev_i32_e32 v1, 31, v0
	v_lshlrev_b64 v[0:1], s45, v[0:1]
	v_lshl_add_u64 v[0:1], v[0:1], 0, s[2:3]
	v_add_f32_e32 v2, v243, v2
	v_lshlrev_b64 v[0:1], 5, v[0:1]
	v_mul_f32_e32 v2, 0x3f317218, v2
	v_lshl_add_u64 v[0:1], s[46:47], 0, v[0:1]
	global_store_dword v[0:1], v2, off

; #define DS_LOADQ(pa) do { const unsigned _q = roff(64 * (c.a0 + (pa)) + 32 * par + r32) + (unsigned)hi * 8u; _Pragma("unroll") for (int d0 = 0; d0 < 8; ++d0) qraw[d0] = *(const u32x2*)(zb + (_q + d0 * 16u)); } while (0)
; __device__ __forceinline__ void datt_stream(LAS unsigned char* lds, const DattRun& c, const float C, const int wv) {
;     ...
;     auto compute = [&](const int rel, const int b, const int pa) __attribute__((always_inline)) {
;         const int tr = edge ? 0 : (rel == 1 ? 1 : (par ? (rel == 0 ? 2 : 0) : (rel == 2 ? 3 : 0))); const bool do0 = tr != 2, do1 = tr != 3;
;         if (rel == 0) {
; #pragma unroll
;             for (int d0 = 0; d0 < 8; ++d0) qr[d0] = f8tob(qraw[d0]); }
;     ...
;             const int st = s + q, dd = st - pa0, rel = dd & 3, pa = pa0 + 4 * (dd >> 2); const bool act = dd >= 0 && pa < NP;
;             if (st > NS) break;
;             if (act && rel <= 2) { compute(rel, q, pa); if (rel == 2 && pa + 4 < NP) DS_LOADQ(pa + 4); }
.LBB0_476:
	s_andn2_b64 vcc, exec, s[6:7]
	s_cbranch_vccnz .LBB0_488
	s_cmp_eq_u32 s98, 0
	s_cbranch_scc1 .LtaN1
	s_mov_b32 s99, 1
	s_branch .LtaE1
.LtaN1:
	s_add_i32 s12, s62, s48
	s_add_i32 s12, s12, s63
	s_lshl_b32 s12, s12, 6
	s_addk_i32 s12, 0xffc0
	s_cmp_lt_u32 s12, s44
	s_cselect_b64 s[10:11], -1, 0
	s_or_b64 s[10:11], s[10:11], s[64:65]
	s_andn2_b64 vcc, exec, s[10:11]
	s_not_b64 s[10:11], s[10:11]
	s_mov_b32 s12, 0
	s_cbranch_vccnz .LBB0_483
	s_cmp_eq_u32 s63, 1
	s_mov_b32 s12, 1
	s_cbranch_scc1 .LBB0_483
	v_readlane_b32 s6, v254, 63
	v_readlane_b32 s7, v255, 0
	s_andn2_b64 vcc, exec, s[6:7]
	s_mov_b64 s[6:7], -1
	s_cbranch_vccnz .LBB0_481
	s_cmp_eq_u32 s63, 0
	s_cselect_b32 s12, 2, 0
	s_mov_b64 s[6:7], 0

; #define DS_LOAD(X, s) do { const int _s = (s) < NS - 1 ? (s) : NS - 1; const int _j = 64 * (c.a0 - 1 + _s) + sr; const unsigned _k0 = DS_KROW(_j) + (unsigned)sc, _k1 = DS_KROW(_j + 32) + (unsigned)sc; \
;         ks##X##0 = *(const u32x2*)(zb + _k0); vs##X##0 = *(const u32x2*)(zb + (_k0 + 1024u)); ks##X##1 = *(const u32x2*)(zb + _k1); vs##X##1 = *(const u32x2*)(zb + (_k1 + 1024u)); } while (0)
; #define DS_WRITE(X, b) do { *(LAS bf16x8*)(V_lds + (b) * SHM_T + vst0) = f8tob(vs##X##0); *(LAS bf16x8*)(K_lds + (b) * SHM_T + kst0) = f8tob(ks##X##0); \
;         *(LAS bf16x8*)(V_lds + (b) * SHM_T + vst1) = f8tob(vs##X##1); *(LAS bf16x8*)(K_lds + (b) * SHM_T + kst1) = f8tob(ks##X##1); } while (0)
; #define DS_LOADQ(pa) do { const unsigned _q = roff(64 * (c.a0 + (pa)) + 32 * par + r32) + (unsigned)hi * 8u; _Pragma("unroll") for (int d0 = 0; d0 < 8; ++d0) qraw[d0] = *(const u32x2*)(zb + (_q + d0 * 16u)); } while (0)
; #define DS_RESET() do { m_reg = -1e30f; l_reg = 0.f; _Pragma("unroll") for (int d = 0; d < 4; ++d) _Pragma("unroll") for (int r = 0; r < 16; ++r) o[d][r] = 0.f; } while (0)
; __device__ __forceinline__ void datt_stream(LAS unsigned char* lds, const DattRun& c, const float C, const int wv) {
;     ...
;     bf16x8 qr[8]; u32x2 qraw[8]; float m_reg = -1e30f, l_reg = 0.f; f32x16 o[4];
;     ...
;     DS_LOADQ(pa0); DS_RESET();
;     auto compute = [&](const int rel, const int b, const int pa) __attribute__((always_inline)) {
;         const int tr = edge ? 0 : (rel == 1 ? 1 : (par ? (rel == 0 ? 2 : 0) : (rel == 2 ? 3 : 0))); const bool do0 = tr != 2, do1 = tr != 3;
;         if (rel == 0) {
; #pragma unroll
;             for (int d0 = 0; d0 < 8; ++d0) qr[d0] = f8tob(qraw[d0]); }
;     ...
;             if (q == 0) { DS_WRITE(A, 1); DS_LOAD(A, st + 3); } else { DS_WRITE(B, 0); DS_LOAD(B, st + 3); }
.LtaE1:
	s_waitcnt vmcnt(6)
	v_cvt_scalef32_pk_bf16_fp8 v66, v212, 1.0
	v_cvt_scalef32_pk_bf16_fp8 v67, v212, 1.0 op_sel:[1,0,0]
	v_cvt_scalef32_pk_bf16_fp8 v68, v213, 1.0
	v_cvt_scalef32_pk_bf16_fp8 v69, v213, 1.0 op_sel:[1,0,0]
	ds_write_b128 v225, v[66:69]
	v_cvt_scalef32_pk_bf16_fp8 v66, v210, 1.0
	v_cvt_scalef32_pk_bf16_fp8 v67, v210, 1.0 op_sel:[1,0,0]
	v_cvt_scalef32_pk_bf16_fp8 v68, v211, 1.0
	v_cvt_scalef32_pk_bf16_fp8 v69, v211, 1.0 op_sel:[1,0,0]
	s_add_i32 s6, s57, 4
	ds_write_b128 v226, v[66:69] offset:32768
	s_waitcnt vmcnt(5)
	s_min_i32 s6, s6, s81
	v_cvt_scalef32_pk_bf16_fp8 v66, v204, 1.0
	v_cvt_scalef32_pk_bf16_fp8 v67, v204, 1.0 op_sel:[1,0,0]
	v_cvt_scalef32_pk_bf16_fp8 v68, v205, 1.0
	v_cvt_scalef32_pk_bf16_fp8 v69, v205, 1.0 op_sel:[1,0,0]
	v_add_u32_e32 v64, s6, v224
	ds_write_b128 v227, v[66:69]
	s_waitcnt vmcnt(4)
	v_lshl_add_u32 v64, v64, 6, v197
	v_cvt_scalef32_pk_bf16_fp8 v66, v200, 1.0
	v_cvt_scalef32_pk_bf16_fp8 v67, v200, 1.0 op_sel:[1,0,0]
	v_cvt_scalef32_pk_bf16_fp8 v68, v201, 1.0
	v_add_u32_e32 v70, 32, v64
	v_min_i32_e32 v70, s95, v70
	v_cmp_lt_i32_e32 vcc, s43, v64
	v_cvt_scalef32_pk_bf16_fp8 v69, v201, 1.0 op_sel:[1,0,0]
	v_min_i32_e32 v72, s95, v64
	s_nop 0
	v_cndmask_b32_e32 v70, 0, v70, vcc
	v_cmp_lt_i32_e32 vcc, -1, v64
	v_lshlrev_b32_e32 v70, s45, v70
	v_add_u32_e32 v70, s56, v70
	v_cndmask_b32_e32 v64, 0, v72, vcc
	v_lshlrev_b32_e32 v64, s45, v64
	v_mad_u64_u32 v[70:71], s[6:7], v70, s42, v[196:197]
	v_add_u32_e32 v64, s56, v64
	v_add_u32_e32 v71, 0x400, v70
	v_mad_u64_u32 v[72:73], s[6:7], v64, s42, v[196:197]
	v_add_u32_e32 v64, 0x400, v72
	global_load_dwordx2 v[204:205], v71, s[92:93]
	global_load_dwordx2 v[212:213], v64, s[92:93]
	global_load_dwordx2 v[210:211], v72, s[92:93]
	global_load_dwordx2 v[200:201], v70, s[92:93]
	ds_write_b128 v228, v[66:69] offset:32768
	s_cmp_eq_u32 s99, 1
	s_cbranch_scc1 .LtaN1
.LtaB1:
	s_cmp_eq_u32 s101, 2
	s_cbranch_scc0 .Ldatt_qc1_skip
	v_cvt_pk_f32_fp8_e32 v[66:67], v176
	v_cvt_pk_f32_fp8_sdwa v[68:69], v176 src0_sel:WORD_1
	v_cvt_pk_f32_fp8_e32 v[70:71], v177
	v_cvt_pk_f32_fp8_sdwa v[72:73], v177 src0_sel:WORD_1
	v_cvt_pk_bf16_f32 v144, v66, v67
	v_cvt_pk_bf16_f32 v145, v68, v69
	v_cvt_pk_bf16_f32 v146, v70, v71
	v_cvt_pk_bf16_f32 v147, v72, v73
	v_cvt_pk_f32_fp8_e32 v[66:67], v178
	v_cvt_pk_f32_fp8_sdwa v[68:69], v178 src0_sel:WORD_1
	v_cvt_pk_f32_fp8_e32 v[70:71], v179
	v_cvt_pk_f32_fp8_sdwa v[72:73], v179 src0_sel:WORD_1
	v_cvt_pk_bf16_f32 v148, v66, v67
	v_cvt_pk_bf16_f32 v149, v68, v69
	v_cvt_pk_bf16_f32 v150, v70, v71
	v_cvt_pk_bf16_f32 v151, v72, v73
	v_cvt_pk_f32_fp8_e32 v[66:67], v180
	v_cvt_pk_f32_fp8_sdwa v[68:69], v180 src0_sel:WORD_1
	v_cvt_pk_f32_fp8_e32 v[70:71], v181
	v_cvt_pk_f32_fp8_sdwa v[72:73], v181 src0_sel:WORD_1
	v_cvt_pk_bf16_f32 v152, v66, v67
	v_cvt_pk_bf16_f32 v153, v68, v69
	v_cvt_pk_bf16_f32 v154, v70, v71
	v_cvt_pk_bf16_f32 v155, v72, v73
	v_cvt_pk_f32_fp8_e32 v[66:67], v182
	v_cvt_pk_f32_fp8_sdwa v[68:69], v182 src0_sel:WORD_1
	v_cvt_pk_f32_fp8_e32 v[70:71], v183
	v_cvt_pk_f32_fp8_sdwa v[72:73], v183 src0_sel:WORD_1
	v_cvt_pk_bf16_f32 v156, v66, v67
	v_cvt_pk_bf16_f32 v157, v68, v69
	v_cvt_pk_bf16_f32 v158, v70, v71
	v_cvt_pk_bf16_f32 v159, v72, v73
	v_cvt_pk_f32_fp8_e32 v[66:67], v184
	v_cvt_pk_f32_fp8_sdwa v[68:69], v184 src0_sel:WORD_1
	v_cvt_pk_f32_fp8_e32 v[70:71], v185
	v_cvt_pk_f32_fp8_sdwa v[72:73], v185 src0_sel:WORD_1
	v_cvt_pk_bf16_f32 v160, v66, v67
	v_cvt_pk_bf16_f32 v161, v68, v69
	v_cvt_pk_bf16_f32 v162, v70, v71
	v_cvt_pk_bf16_f32 v163, v72, v73
	v_cvt_pk_f32_fp8_e32 v[66:67], v188
	v_cvt_pk_f32_fp8_sdwa v[68:69], v188 src0_sel:WORD_1
	v_cvt_pk_f32_fp8_e32 v[70:71], v189
	v_cvt_pk_f32_fp8_sdwa v[72:73], v189 src0_sel:WORD_1
	v_cvt_pk_bf16_f32 v164, v66, v67
	v_cvt_pk_bf16_f32 v165, v68, v69
	v_cvt_pk_bf16_f32 v166, v70, v71
	v_cvt_pk_bf16_f32 v167, v72, v73
	v_cvt_pk_f32_fp8_e32 v[66:67], v190
	v_cvt_pk_f32_fp8_sdwa v[68:69], v190 src0_sel:WORD_1
	v_cvt_pk_f32_fp8_e32 v[70:71], v191
	v_cvt_pk_f32_fp8_sdwa v[72:73], v191 src0_sel:WORD_1
	v_cvt_pk_bf16_f32 v168, v66, v67
	v_cvt_pk_bf16_f32 v169, v68, v69
	v_cvt_pk_bf16_f32 v170, v70, v71
	v_cvt_pk_bf16_f32 v171, v72, v73
	v_cvt_pk_f32_fp8_e32 v[66:67], v192
	v_cvt_pk_f32_fp8_sdwa v[68:69], v192 src0_sel:WORD_1
	v_cvt_pk_f32_fp8_e32 v[70:71], v193
	v_cvt_pk_f32_fp8_sdwa v[72:73], v193 src0_sel:WORD_1
	v_cvt_pk_bf16_f32 v172, v66, v67
	v_cvt_pk_bf16_f32 v173, v68, v69
	v_cvt_pk_bf16_f32 v174, v70, v71
	v_cvt_pk_bf16_f32 v175, v72, v73
	s_mov_b32 s101, 3
